# chunk phase A-matrix tile epilogues: the per-element ds_read_b32 pairs (decay/beta) issued in one batch after the tile's MFMAs instead of one LDS round trip per element; per-element lgkmcnt waits drop
# baseline (speedup 1.0000x reference)
.LBB0_417:
	s_andn2_b64 vcc, exec, s[6:7]
	s_cbranch_vccnz .LBB0_419
	s_waitcnt vmcnt(15)
	v_lshlrev_b32_e32 v0, 3, v75
	v_lshlrev_b32_e32 v1, 8, v73
	v_lshlrev_b32_e32 v0, 1, v0
	s_waitcnt vmcnt(11)
	v_add3_u32 v25, s27, v1, v0
	s_waitcnt vmcnt(10)
	ds_read_b128 v[26:29], v25 offset:17408
	ds_read_b128 v[30:33], v25 offset:17440
	ds_read_b128 v[34:37], v25 offset:17472
	ds_read_b128 v[38:41], v25 offset:17504
	s_waitcnt lgkmcnt(3)
	v_mfma_f32_32x32x16_bf16 v[0:15], v[26:29], v[26:29], 0
	s_waitcnt vmcnt(8)
	v_lshl_add_u32 v16, v75, 10, s27
	s_movk_i32 s2, 0xfc10
	v_mad_i32_i24 v96, v75, s2, v16
	ds_read_b32 v17, v96 offset:16640
	v_lshl_add_u32 v24, v73, 2, v16
	v_sub_u32_e32 v16, v47, v73
	v_cmp_lt_i32_e32 vcc, 0, v16
	s_waitcnt lgkmcnt(3)
	v_mfma_f32_32x32x16_bf16 v[0:15], v[30:33], v[30:33], v[0:15]
	s_movk_i32 s2, 0xffe1
	v_sub_u32_e32 v47, v47, v71
	s_waitcnt lgkmcnt(2)
	v_mfma_f32_32x32x16_bf16 v[0:15], v[34:37], v[34:37], v[0:15]
	s_waitcnt lgkmcnt(1)
	v_mfma_f32_32x32x16_bf16 v[0:15], v[38:41], v[38:41], v[0:15]
	ds_read_b32 v100, v96 offset:16384
	ds_read_b32 v101, v96 offset:16644
	ds_read_b32 v102, v96 offset:16388
	ds_read_b32 v103, v96 offset:16648
	ds_read_b32 v104, v96 offset:16392
	ds_read_b32 v105, v96 offset:16652
	ds_read_b32 v106, v96 offset:16396
	ds_read_b32 v107, v96 offset:16672
	ds_read_b32 v108, v96 offset:16416
	ds_read_b32 v109, v96 offset:16676
	ds_read_b32 v110, v96 offset:16420
	ds_read_b32 v111, v96 offset:16680
	ds_read_b32 v114, v96 offset:16424
	ds_read_b32 v115, v96 offset:16684
	ds_read_b32 v116, v96 offset:16428
	ds_read_b32 v117, v96 offset:16704
	ds_read_b32 v118, v96 offset:16448
	ds_read_b32 v119, v96 offset:16708
	ds_read_b32 v120, v96 offset:16452
	ds_read_b32 v121, v96 offset:16712
	ds_read_b32 v122, v96 offset:16456
	ds_read_b32 v123, v96 offset:16716
	ds_read_b32 v124, v96 offset:16460
	ds_read_b32 v125, v96 offset:16736
	ds_read_b32 v126, v96 offset:16480
	ds_read_b32 v127, v96 offset:16740
	ds_read_b32 v128, v96 offset:16484
	ds_read_b32 v129, v96 offset:16744
	ds_read_b32 v130, v96 offset:16488
	ds_read_b32 v131, v96 offset:16748
	ds_read_b32 v132, v96 offset:16492
	s_waitcnt lgkmcnt(0)
	s_nop 10
	v_mul_f32_e32 v0, v0, v17
	v_sub_f32_e32 v17, v100, v74
	v_min_f32_e32 v17, 0, v17
	v_mul_f32_e32 v17, 0x3fb8aa3b, v17
	v_exp_f32_e32 v17, v17
	s_nop 0
	v_mul_f32_e32 v0, v0, v17
	v_cndmask_b32_e32 v0, 0, v0, vcc
	ds_write_b32 v24, v0
	v_cmp_gt_u32_e32 vcc, s2, v16
	s_movk_i32 s2, 0xffef
	v_mul_f32_e32 v0, v1, v101
	v_sub_f32_e32 v1, v102, v74
	v_min_f32_e32 v1, 0, v1
	v_mul_f32_e32 v1, 0x3fb8aa3b, v1
	v_exp_f32_e32 v1, v1
	s_nop 0
	v_mul_f32_e32 v0, v0, v1
	v_cndmask_b32_e32 v0, 0, v0, vcc
	ds_write_b32 v24, v0 offset:256
	v_cmp_lt_i32_e32 vcc, -2, v16
	v_mul_f32_e32 v0, v2, v103
	v_sub_f32_e32 v1, v104, v74
	v_min_f32_e32 v1, 0, v1
	v_mul_f32_e32 v1, 0x3fb8aa3b, v1
	v_exp_f32_e32 v1, v1
	s_nop 0
	v_mul_f32_e32 v0, v0, v1
	v_cndmask_b32_e32 v0, 0, v0, vcc
	ds_write_b32 v24, v0 offset:512
	v_cmp_lt_i32_e32 vcc, -3, v16
	v_mul_f32_e32 v0, v3, v105
	v_sub_f32_e32 v1, v106, v74
	v_min_f32_e32 v1, 0, v1
	v_mul_f32_e32 v1, 0x3fb8aa3b, v1
	v_exp_f32_e32 v1, v1
	s_nop 0
	v_mul_f32_e32 v0, v0, v1
	v_cndmask_b32_e32 v0, 0, v0, vcc
	ds_write_b32 v24, v0 offset:768
	v_cmp_lt_i32_e32 vcc, -8, v16
	v_mul_f32_e32 v0, v4, v107
	v_sub_f32_e32 v1, v108, v74
	v_min_f32_e32 v1, 0, v1
	v_mul_f32_e32 v1, 0x3fb8aa3b, v1
	v_exp_f32_e32 v1, v1
	s_nop 0
	v_mul_f32_e32 v0, v0, v1
	v_cndmask_b32_e32 v0, 0, v0, vcc
	ds_write_b32 v24, v0 offset:2048
	v_cmp_lt_i32_e32 vcc, -9, v16
	v_mul_f32_e32 v0, v5, v109
	v_sub_f32_e32 v1, v110, v74
	v_min_f32_e32 v1, 0, v1
	v_mul_f32_e32 v1, 0x3fb8aa3b, v1
	v_exp_f32_e32 v1, v1
	s_nop 0
	v_mul_f32_e32 v0, v0, v1
	v_cndmask_b32_e32 v0, 0, v0, vcc
	ds_write_b32 v24, v0 offset:2304
	v_cmp_lt_i32_e32 vcc, -10, v16
	v_mul_f32_e32 v0, v6, v111
	v_sub_f32_e32 v1, v114, v74
	v_min_f32_e32 v1, 0, v1
	v_mul_f32_e32 v1, 0x3fb8aa3b, v1
	v_exp_f32_e32 v1, v1
	s_nop 0
	v_mul_f32_e32 v0, v0, v1
	v_cndmask_b32_e32 v0, 0, v0, vcc
	ds_write_b32 v24, v0 offset:2560
	v_cmp_lt_i32_e32 vcc, -11, v16
	v_mul_f32_e32 v0, v7, v115
	v_sub_f32_e32 v1, v116, v74
	v_min_f32_e32 v1, 0, v1
	v_mul_f32_e32 v1, 0x3fb8aa3b, v1
	v_exp_f32_e32 v1, v1
	s_nop 0
	v_mul_f32_e32 v0, v0, v1
	v_cndmask_b32_e32 v0, 0, v0, vcc
	ds_write_b32 v24, v0 offset:2816
	v_cmp_lt_i32_e32 vcc, -16, v16
	v_mul_f32_e32 v0, v8, v117
	v_sub_f32_e32 v1, v118, v74
	v_min_f32_e32 v1, 0, v1
	v_mul_f32_e32 v1, 0x3fb8aa3b, v1
	v_exp_f32_e32 v1, v1
	s_nop 0
	v_mul_f32_e32 v0, v0, v1
	v_cndmask_b32_e32 v0, 0, v0, vcc
	ds_write_b32 v24, v0 offset:4096
	v_cmp_lt_i32_e32 vcc, s2, v16
	s_movk_i32 s2, 0xffee
	v_mul_f32_e32 v0, v9, v119
	v_sub_f32_e32 v1, v120, v74
	v_min_f32_e32 v1, 0, v1
	v_mul_f32_e32 v1, 0x3fb8aa3b, v1
	v_exp_f32_e32 v1, v1
	s_nop 0
	v_mul_f32_e32 v0, v0, v1
	v_cndmask_b32_e32 v0, 0, v0, vcc
	ds_write_b32 v24, v0 offset:4352
	v_cmp_lt_i32_e32 vcc, s2, v16
	s_movk_i32 s2, 0xffed
	v_mul_f32_e32 v0, v10, v121
	v_sub_f32_e32 v1, v122, v74
	v_min_f32_e32 v1, 0, v1
	v_mul_f32_e32 v1, 0x3fb8aa3b, v1
	v_exp_f32_e32 v1, v1
	s_nop 0
	v_mul_f32_e32 v0, v0, v1
	v_cndmask_b32_e32 v0, 0, v0, vcc
	ds_write_b32 v24, v0 offset:4608
	v_cmp_lt_i32_e32 vcc, s2, v16
	s_movk_i32 s2, 0xffe8
	v_mul_f32_e32 v0, v11, v123
	v_sub_f32_e32 v1, v124, v74
	v_min_f32_e32 v1, 0, v1
	v_mul_f32_e32 v1, 0x3fb8aa3b, v1
	v_exp_f32_e32 v1, v1
	s_nop 0
	v_mul_f32_e32 v0, v0, v1
	v_cndmask_b32_e32 v0, 0, v0, vcc
	ds_write_b32 v24, v0 offset:4864
	v_cmp_lt_i32_e32 vcc, s2, v16
	s_movk_i32 s2, 0xffe7
	v_mul_f32_e32 v0, v12, v125
	v_sub_f32_e32 v1, v126, v74
	v_min_f32_e32 v1, 0, v1
	v_mul_f32_e32 v1, 0x3fb8aa3b, v1
	v_exp_f32_e32 v1, v1
	s_nop 0
	v_mul_f32_e32 v0, v0, v1
	v_cndmask_b32_e32 v0, 0, v0, vcc
	ds_write_b32 v24, v0 offset:6144
	v_cmp_lt_i32_e32 vcc, s2, v16
	s_movk_i32 s2, 0xffe6
	v_mul_f32_e32 v0, v13, v127
	v_sub_f32_e32 v1, v128, v74
	v_min_f32_e32 v1, 0, v1
	v_mul_f32_e32 v1, 0x3fb8aa3b, v1
	v_exp_f32_e32 v1, v1
	s_nop 0
	v_mul_f32_e32 v0, v0, v1
	v_cndmask_b32_e32 v0, 0, v0, vcc
	ds_write_b32 v24, v0 offset:6400
	v_cmp_lt_i32_e32 vcc, s2, v16
	s_movk_i32 s2, 0xffe5
	v_mul_f32_e32 v0, v14, v129
	v_sub_f32_e32 v1, v130, v74
	v_min_f32_e32 v1, 0, v1
	v_mul_f32_e32 v1, 0x3fb8aa3b, v1
	v_exp_f32_e32 v1, v1
	s_nop 0
	v_mul_f32_e32 v0, v0, v1
	v_cndmask_b32_e32 v0, 0, v0, vcc
	ds_write_b32 v24, v0 offset:6656
	v_cmp_lt_i32_e32 vcc, s2, v16
	s_movk_i32 s2, 0xffe0
	v_mul_f32_e32 v0, v15, v131
	v_sub_f32_e32 v1, v132, v74
	v_min_f32_e32 v1, 0, v1
	v_mul_f32_e32 v1, 0x3fb8aa3b, v1
	v_exp_f32_e32 v1, v1
	s_nop 0
	v_mul_f32_e32 v0, v0, v1
	v_cndmask_b32_e32 v0, 0, v0, vcc
	ds_write_b32 v24, v0 offset:6912
	ds_read_b32 v78, v96 offset:16800
	ds_read_b128 v[16:19], v96 offset:16512
	ds_read_b128 v[20:23], v96 offset:16768
	ds_read_b128 v[80:83], v25 offset:25696
	ds_read_b128 v[84:87], v25 offset:25664
	ds_read_b128 v[88:91], v25 offset:25600
	ds_read_b128 v[92:95], v25 offset:25632
	s_waitcnt lgkmcnt(1)
	v_mfma_f32_32x32x16_bf16 v[0:15], v[88:91], v[26:29], 0
	v_sub_f32_e32 v25, v16, v74
	v_min_f32_e32 v25, 0, v25
	v_mul_f32_e32 v25, 0x3fb8aa3b, v25
	v_exp_f32_e32 v25, v25
	v_cmp_lt_u32_e32 vcc, s2, v47
	s_movk_i32 s2, 0xffdf
	ds_read_b32 v72, v72 offset:16512
	s_waitcnt lgkmcnt(1)
	v_mfma_f32_32x32x16_bf16 v[0:15], v[92:95], v[30:33], v[0:15]
	s_waitcnt lgkmcnt(0)
	v_sub_f32_e32 v16, v16, v72
	v_min_f32_e32 v16, 0, v16
	v_mul_f32_e32 v16, 0x3fb8aa3b, v16
	v_exp_f32_e32 v16, v16
	v_mfma_f32_32x32x16_bf16 v[0:15], v[84:87], v[34:37], v[0:15]
	v_mfma_f32_32x32x16_bf16 v[0:15], v[80:83], v[38:41], v[0:15]
	ds_read_b32 v133, v96 offset:16544
	ds_read_b32 v134, v96 offset:16804
	ds_read_b32 v135, v96 offset:16548
	ds_read_b32 v136, v96 offset:16808
	ds_read_b32 v137, v96 offset:16552
	ds_read_b32 v138, v96 offset:16812
	ds_read_b32 v139, v96 offset:16556
	ds_read_b32 v140, v96 offset:16832
	ds_read_b32 v141, v96 offset:16576
	ds_read_b32 v142, v96 offset:16836
	ds_read_b32 v143, v96 offset:16580
	ds_read_b32 v144, v96 offset:16840
	ds_read_b32 v145, v96 offset:16584
	ds_read_b32 v146, v96 offset:16844
	ds_read_b32 v147, v96 offset:16588
	ds_read_b32 v148, v96 offset:16864
	ds_read_b32 v149, v96 offset:16608
	ds_read_b32 v150, v96 offset:16868
	ds_read_b32 v151, v96 offset:16612
	ds_read_b32 v152, v96 offset:16872
	ds_read_b32 v153, v96 offset:16616
	ds_read_b32 v154, v96 offset:16876
	ds_read_b32 v155, v96 offset:16620
	s_waitcnt lgkmcnt(0)
	s_nop 11
	v_mul_f32_e32 v0, v20, v0
	v_mul_f32_e32 v0, v25, v0
	ds_write_b32 v24, v0 offset:8192
	v_mul_f32_e32 v0, v21, v1
	v_sub_f32_e32 v1, v17, v74
	v_min_f32_e32 v1, 0, v1
	v_mul_f32_e32 v1, 0x3fb8aa3b, v1
	v_exp_f32_e32 v1, v1
	s_nop 0
	v_mul_f32_e32 v0, v1, v0
	v_sub_f32_e32 v1, v18, v74
	v_min_f32_e32 v1, 0, v1
	v_mul_f32_e32 v1, 0x3fb8aa3b, v1
	v_exp_f32_e32 v1, v1
	ds_write_b32 v24, v0 offset:8448
	v_mul_f32_e32 v0, v22, v2
	v_mul_f32_e32 v0, v1, v0
	v_sub_f32_e32 v1, v19, v74
	v_min_f32_e32 v1, 0, v1
	v_mul_f32_e32 v1, 0x3fb8aa3b, v1
	v_exp_f32_e32 v1, v1
	ds_write_b32 v24, v0 offset:8704
	v_mul_f32_e32 v0, v23, v3
	v_mul_f32_e32 v0, v1, v0
	ds_write_b32 v24, v0 offset:8960
	v_mul_f32_e32 v0, v78, v4
	v_sub_f32_e32 v1, v133, v74
	v_min_f32_e32 v1, 0, v1
	v_mul_f32_e32 v1, 0x3fb8aa3b, v1
	v_exp_f32_e32 v1, v1
	s_nop 0
	v_mul_f32_e32 v0, v0, v1
	ds_write_b32 v24, v0 offset:10240
	v_mul_f32_e32 v0, v5, v134
	v_sub_f32_e32 v1, v135, v74
	v_min_f32_e32 v1, 0, v1
	v_mul_f32_e32 v1, 0x3fb8aa3b, v1
	v_exp_f32_e32 v1, v1
	s_nop 0
	v_mul_f32_e32 v0, v0, v1
	ds_write_b32 v24, v0 offset:10496
	v_mul_f32_e32 v0, v6, v136
	v_sub_f32_e32 v1, v137, v74
	v_min_f32_e32 v1, 0, v1
	v_mul_f32_e32 v1, 0x3fb8aa3b, v1
	v_exp_f32_e32 v1, v1
	s_nop 0
	v_mul_f32_e32 v0, v0, v1
	ds_write_b32 v24, v0 offset:10752
	v_mul_f32_e32 v0, v7, v138
	v_sub_f32_e32 v1, v139, v74
	v_min_f32_e32 v1, 0, v1
	v_mul_f32_e32 v1, 0x3fb8aa3b, v1
	v_exp_f32_e32 v1, v1
	s_nop 0
	v_mul_f32_e32 v0, v0, v1
	ds_write_b32 v24, v0 offset:11008
	v_mul_f32_e32 v0, v8, v140
	v_sub_f32_e32 v1, v141, v74
	v_min_f32_e32 v1, 0, v1
	v_mul_f32_e32 v1, 0x3fb8aa3b, v1
	v_exp_f32_e32 v1, v1
	s_nop 0
	v_mul_f32_e32 v0, v0, v1
	ds_write_b32 v24, v0 offset:12288
	v_mul_f32_e32 v0, v9, v142
	v_sub_f32_e32 v1, v143, v74
	v_min_f32_e32 v1, 0, v1
	v_mul_f32_e32 v1, 0x3fb8aa3b, v1
	v_exp_f32_e32 v1, v1
	s_nop 0
	v_mul_f32_e32 v0, v0, v1
	ds_write_b32 v24, v0 offset:12544
	v_mul_f32_e32 v0, v10, v144
	v_sub_f32_e32 v1, v145, v74
	v_min_f32_e32 v1, 0, v1
	v_mul_f32_e32 v1, 0x3fb8aa3b, v1
	v_exp_f32_e32 v1, v1
	s_nop 0
	v_mul_f32_e32 v0, v0, v1
	ds_write_b32 v24, v0 offset:12800
	v_mul_f32_e32 v0, v11, v146
	v_sub_f32_e32 v1, v147, v74
	v_min_f32_e32 v1, 0, v1
	v_mul_f32_e32 v1, 0x3fb8aa3b, v1
	v_exp_f32_e32 v1, v1
	s_nop 0
	v_mul_f32_e32 v0, v0, v1
	ds_write_b32 v24, v0 offset:13056
	v_mul_f32_e32 v0, v12, v148
	v_sub_f32_e32 v1, v149, v74
	v_min_f32_e32 v1, 0, v1
	v_mul_f32_e32 v1, 0x3fb8aa3b, v1
	v_exp_f32_e32 v1, v1
	s_nop 0
	v_mul_f32_e32 v0, v0, v1
	ds_write_b32 v24, v0 offset:14336
	v_mul_f32_e32 v0, v13, v150
	v_sub_f32_e32 v1, v151, v74
	v_min_f32_e32 v1, 0, v1
	v_mul_f32_e32 v1, 0x3fb8aa3b, v1
	v_exp_f32_e32 v1, v1
	s_nop 0
	v_mul_f32_e32 v0, v0, v1
	ds_write_b32 v24, v0 offset:14592
	v_mul_f32_e32 v0, v14, v152
	v_sub_f32_e32 v1, v153, v74
	v_min_f32_e32 v1, 0, v1
	v_mul_f32_e32 v1, 0x3fb8aa3b, v1
	v_exp_f32_e32 v1, v1
	s_nop 0
	v_mul_f32_e32 v0, v0, v1
	ds_write_b32 v24, v0 offset:14848
	v_mul_f32_e32 v0, v15, v154
	v_sub_f32_e32 v1, v155, v74
	v_min_f32_e32 v1, 0, v1
	v_mul_f32_e32 v1, 0x3fb8aa3b, v1
	v_exp_f32_e32 v1, v1
	s_nop 0
	v_mul_f32_e32 v27, v0, v1
	v_mfma_f32_32x32x16_bf16 v[0:15], v[88:91], v[88:91], 0
	v_mfma_f32_32x32x16_bf16 v[0:15], v[92:95], v[92:95], v[0:15]
	v_mfma_f32_32x32x16_bf16 v[0:15], v[84:87], v[84:87], v[0:15]
	v_mfma_f32_32x32x16_bf16 v[0:15], v[80:83], v[80:83], v[0:15]
	s_nop 11
	v_mul_f32_e32 v0, v20, v0
	v_mul_f32_e32 v0, v0, v16
	v_cndmask_b32_e32 v0, 0, v0, vcc
	ds_write_b32 v24, v0 offset:8320
	v_mul_f32_e32 v0, v21, v1
	v_sub_f32_e32 v1, v17, v72
	v_min_f32_e32 v1, 0, v1
	v_mul_f32_e32 v1, 0x3fb8aa3b, v1
	v_exp_f32_e32 v1, v1
	v_cmp_lt_u32_e32 vcc, s2, v47
	s_movk_i32 s2, 0xffde
	v_mul_f32_e32 v0, v0, v1
	v_sub_f32_e32 v1, v18, v72
	v_min_f32_e32 v1, 0, v1
	v_mul_f32_e32 v1, 0x3fb8aa3b, v1
	v_exp_f32_e32 v1, v1
	v_cndmask_b32_e32 v0, 0, v0, vcc
	ds_write_b32 v24, v0 offset:8576
	v_mul_f32_e32 v0, v22, v2
	v_mul_f32_e32 v0, v0, v1
	v_sub_f32_e32 v1, v19, v72
	v_min_f32_e32 v1, 0, v1
	v_mul_f32_e32 v1, 0x3fb8aa3b, v1
	v_exp_f32_e32 v1, v1
	v_cmp_lt_u32_e32 vcc, s2, v47
	s_movk_i32 s2, 0xffdd
	s_nop 0
	v_cndmask_b32_e32 v0, 0, v0, vcc
	ds_write_b32 v24, v0 offset:8832
	v_mul_f32_e32 v0, v23, v3
	v_mul_f32_e32 v0, v0, v1
	v_sub_f32_e32 v1, v133, v72
	v_min_f32_e32 v1, 0, v1
	v_mul_f32_e32 v1, 0x3fb8aa3b, v1
	v_exp_f32_e32 v1, v1
	v_cmp_lt_u32_e32 vcc, s2, v47
	s_movk_i32 s2, 0xffd8
	s_nop 0
	v_cndmask_b32_e32 v0, 0, v0, vcc
	ds_write_b32 v24, v0 offset:9088
	v_mul_f32_e32 v0, v78, v4
	v_mul_f32_e32 v0, v0, v1
	v_sub_f32_e32 v1, v135, v72
	v_min_f32_e32 v1, 0, v1
	v_mul_f32_e32 v1, 0x3fb8aa3b, v1
	v_exp_f32_e32 v1, v1
	v_cmp_lt_u32_e32 vcc, s2, v47
	s_movk_i32 s2, 0xffd7
	s_nop 0
	v_cndmask_b32_e32 v0, 0, v0, vcc
	ds_write_b32 v24, v0 offset:10368
	v_mul_f32_e32 v0, v134, v5
	v_mul_f32_e32 v0, v0, v1
	v_sub_f32_e32 v1, v137, v72
	v_min_f32_e32 v1, 0, v1
	v_mul_f32_e32 v1, 0x3fb8aa3b, v1
	v_exp_f32_e32 v1, v1
	v_cmp_lt_u32_e32 vcc, s2, v47
	s_movk_i32 s2, 0xffd6
	s_nop 0
	v_cndmask_b32_e32 v0, 0, v0, vcc
	ds_write_b32 v24, v0 offset:10624
	v_mul_f32_e32 v0, v136, v6
	v_mul_f32_e32 v0, v0, v1
	v_sub_f32_e32 v1, v139, v72
	v_min_f32_e32 v1, 0, v1
	v_mul_f32_e32 v1, 0x3fb8aa3b, v1
	v_exp_f32_e32 v1, v1
	v_cmp_lt_u32_e32 vcc, s2, v47
	s_movk_i32 s2, 0xffd5
	s_nop 0
	v_cndmask_b32_e32 v0, 0, v0, vcc
	ds_write_b32 v24, v0 offset:10880
	v_mul_f32_e32 v0, v138, v7
	v_mul_f32_e32 v0, v0, v1
	v_sub_f32_e32 v1, v141, v72
	v_min_f32_e32 v1, 0, v1
	v_mul_f32_e32 v1, 0x3fb8aa3b, v1
	v_exp_f32_e32 v1, v1
	v_cmp_lt_u32_e32 vcc, s2, v47
	s_movk_i32 s2, 0xffd0
	s_nop 0
	v_cndmask_b32_e32 v0, 0, v0, vcc
	ds_write_b32 v24, v0 offset:11136
	v_mul_f32_e32 v0, v140, v8
	v_mul_f32_e32 v0, v0, v1
	v_sub_f32_e32 v1, v143, v72
	v_min_f32_e32 v1, 0, v1
	v_mul_f32_e32 v1, 0x3fb8aa3b, v1
	v_exp_f32_e32 v1, v1
	v_cmp_lt_u32_e32 vcc, s2, v47
	s_movk_i32 s2, 0xffcf
	s_nop 0
	v_cndmask_b32_e32 v0, 0, v0, vcc
	ds_write_b32 v24, v0 offset:12416
	v_mul_f32_e32 v0, v142, v9
	v_mul_f32_e32 v0, v0, v1
	v_sub_f32_e32 v1, v145, v72
	v_min_f32_e32 v1, 0, v1
	v_mul_f32_e32 v1, 0x3fb8aa3b, v1
	v_exp_f32_e32 v1, v1
	v_cmp_lt_u32_e32 vcc, s2, v47
	s_movk_i32 s2, 0xffce
	s_nop 0
	v_cndmask_b32_e32 v0, 0, v0, vcc
	ds_write_b32 v24, v0 offset:12672
	v_mul_f32_e32 v0, v144, v10
	v_mul_f32_e32 v0, v0, v1
	v_sub_f32_e32 v1, v147, v72
	v_min_f32_e32 v1, 0, v1
	v_mul_f32_e32 v1, 0x3fb8aa3b, v1
	v_exp_f32_e32 v1, v1
	v_cmp_lt_u32_e32 vcc, s2, v47
	s_movk_i32 s2, 0xffcd
	s_nop 0
	v_cndmask_b32_e32 v0, 0, v0, vcc
	ds_write_b32 v24, v0 offset:12928
	v_mul_f32_e32 v0, v146, v11
	v_mul_f32_e32 v0, v0, v1
	v_sub_f32_e32 v1, v149, v72
	v_min_f32_e32 v1, 0, v1
	v_mul_f32_e32 v1, 0x3fb8aa3b, v1
	v_exp_f32_e32 v1, v1
	v_cmp_lt_u32_e32 vcc, s2, v47
	s_movk_i32 s2, 0xffc8
	s_nop 0
	v_cndmask_b32_e32 v0, 0, v0, vcc
	ds_write_b32 v24, v0 offset:13184
	v_mul_f32_e32 v0, v148, v12
	v_mul_f32_e32 v0, v0, v1
	v_sub_f32_e32 v1, v151, v72
	v_min_f32_e32 v1, 0, v1
	v_mul_f32_e32 v1, 0x3fb8aa3b, v1
	v_exp_f32_e32 v1, v1
	v_cmp_lt_u32_e32 vcc, s2, v47
	s_movk_i32 s2, 0xffc7
	s_nop 0
	v_cndmask_b32_e32 v0, 0, v0, vcc
	ds_write_b32 v24, v0 offset:14464
	v_mul_f32_e32 v0, v150, v13
	v_mul_f32_e32 v0, v0, v1
	v_sub_f32_e32 v1, v153, v72
	v_min_f32_e32 v1, 0, v1
	v_mul_f32_e32 v1, 0x3fb8aa3b, v1
	v_exp_f32_e32 v1, v1
	v_cmp_lt_u32_e32 vcc, s2, v47
	s_movk_i32 s2, 0xffc6
	s_nop 0
	v_cndmask_b32_e32 v0, 0, v0, vcc
	ds_write_b32 v24, v0 offset:14720
	v_mul_f32_e32 v0, v152, v14
	v_mul_f32_e32 v0, v0, v1
	v_cmp_lt_u32_e32 vcc, s2, v47
	v_add_u32_e32 v1, 0x3800, v24
	s_movk_i32 s2, 0xffc5
	v_cndmask_b32_e32 v0, 0, v0, vcc
	ds_write2_b32 v1, v0, v27 offset0:160 offset1:192
	v_sub_f32_e32 v1, v155, v72
	v_min_f32_e32 v1, 0, v1
	v_mul_f32_e32 v1, 0x3fb8aa3b, v1
	v_exp_f32_e32 v1, v1
	v_mul_f32_e32 v0, v154, v15
	v_cmp_lt_u32_e32 vcc, s2, v47
	v_mul_f32_e32 v0, v0, v1
	s_nop 0
	v_cndmask_b32_e32 v0, 0, v0, vcc
	ds_write_b32 v24, v0 offset:15232
